# baseline (speedup 1.0000x reference)
.Lfast0:
	v_cvt_pk_f16_f32 v180, v46, v47
	v_cvt_pk_f16_f32 v181, v48, v49
	v_mfma_f32_16x16x32_f16 v[6:9], a[0:3], v[224:227], v[6:9]
	v_and_b32_dpp v228, v62, v167 row_ror:8 row_mask:0xf bank_mask:0xf
	v_and_b32_dpp v229, v63, v167 row_ror:8 row_mask:0xf bank_mask:0xf
	v_mfma_f32_16x16x32_f16 v[10:13], a[32:35], v[224:227], v[10:13]
	v_and_b32_dpp v230, v64, v167 row_ror:8 row_mask:0xf bank_mask:0xf
	v_and_b32_dpp v231, v65, v167 row_ror:8 row_mask:0xf bank_mask:0xf
	v_mfma_f32_16x16x32_f16 v[14:17], a[64:67], v[224:227], v[14:17]
	v_cvt_pk_f16_f32 v182, v50, v51
	v_cvt_pk_f16_f32 v183, v52, v53
	v_mfma_f32_16x16x32_f16 v[18:21], a[96:99], v[224:227], v[18:21]
	v_cvt_pk_f16_f32 v218, v38, v39
	v_cvt_pk_f16_f32 v219, v40, v41
	v_mfma_f32_16x16x32_f16 v[22:25], a[128:131], v[224:227], v[22:25]
	s_waitcnt vmcnt(2)
	v_mfma_f32_16x16x32_f16 v[26:29], a[160:163], v[224:227], v[26:29]
	v_bitop3_b32 v168, v66, v67, s30 bitop3:0x7e
	v_bitop3_b32 v169, v68, v69, s30 bitop3:0x7e
	v_mfma_f32_16x16x32_f16 v[30:33], a[192:195], v[224:227], v[30:33]
	v_bitop3_b32 v168, v168, v169, s18 bitop3:0xa8
	v_cmp_ne_u32_e32 vcc, 0, v168
	v_mfma_f32_16x16x32_f16 v[34:37], a[224:227], v[224:227], v[34:37]
	v_and_b32_e32 v232, v66, v167
	v_and_b32_e32 v233, v67, v167
	v_mfma_f32_16x16x32_f16 v[6:9], a[4:7], v[228:231], v[6:9]
	v_and_b32_e32 v234, v68, v167
	v_and_b32_e32 v235, v69, v167
	v_mfma_f32_16x16x32_f16 v[10:13], a[36:39], v[228:231], v[10:13]
	v_cvt_pk_f16_f32 v220, v42, v43
	v_cvt_pk_f16_f32 v221, v44, v45
	v_mfma_f32_16x16x32_f16 v[14:17], a[68:71], v[228:231], v[14:17]
	v_mfma_f32_16x16x32_f16 v[18:21], a[100:103], v[228:231], v[18:21]
	v_mfma_f32_16x16x32_f16 v[22:25], a[132:135], v[228:231], v[22:25]
	v_mfma_f32_16x16x32_f16 v[26:29], a[164:167], v[228:231], v[26:29]
	v_mfma_f32_16x16x32_f16 v[30:33], a[196:199], v[228:231], v[30:33]
	v_mfma_f32_16x16x32_f16 v[34:37], a[228:231], v[228:231], v[34:37]
	s_cbranch_vccnz .Lrestart1
.Lfast1:
	v_mfma_f32_16x16x32_f16 v[6:9], a[8:11], v[232:235], v[6:9]
	v_and_b32_dpp v236, v66, v167 row_ror:8 row_mask:0xf bank_mask:0xf
	v_and_b32_dpp v237, v67, v167 row_ror:8 row_mask:0xf bank_mask:0xf
	v_mfma_f32_16x16x32_f16 v[10:13], a[40:43], v[232:235], v[10:13]
	v_and_b32_dpp v238, v68, v167 row_ror:8 row_mask:0xf bank_mask:0xf
	v_and_b32_dpp v239, v69, v167 row_ror:8 row_mask:0xf bank_mask:0xf
	v_mfma_f32_16x16x32_f16 v[14:17], a[72:75], v[232:235], v[14:17]
	v_xor_b32_e32 v222, 0x4000, v222
	ds_read_b128 v[130:133], v222
	v_mfma_f32_16x16x32_f16 v[18:21], a[104:107], v[232:235], v[18:21]
	ds_read_b128 v[126:129], v222 offset:1024
	ds_read_b128 v[122:125], v222 offset:2048
	v_mfma_f32_16x16x32_f16 v[22:25], a[136:139], v[232:235], v[22:25]
	s_waitcnt vmcnt(1)
	v_mfma_f32_16x16x32_f16 v[26:29], a[168:171], v[232:235], v[26:29]
	v_bitop3_b32 v168, v70, v71, s30 bitop3:0x7e
	v_bitop3_b32 v169, v72, v73, s30 bitop3:0x7e
	v_mfma_f32_16x16x32_f16 v[30:33], a[200:203], v[232:235], v[30:33]
	v_bitop3_b32 v168, v168, v169, s18 bitop3:0xa8
	v_cmp_ne_u32_e32 vcc, 0, v168
	v_mfma_f32_16x16x32_f16 v[34:37], a[232:235], v[232:235], v[34:37]
	v_and_b32_e32 v240, v70, v167
	v_and_b32_e32 v241, v71, v167
	v_mfma_f32_16x16x32_f16 v[6:9], a[12:15], v[236:239], v[6:9]
	v_and_b32_e32 v242, v72, v167
	v_and_b32_e32 v243, v73, v167
	v_mfma_f32_16x16x32_f16 v[10:13], a[44:47], v[236:239], v[10:13]
	ds_read_b128 v[118:121], v222 offset:3072
	ds_read_b128 v[114:117], v222 offset:4096
	v_mfma_f32_16x16x32_f16 v[14:17], a[76:79], v[236:239], v[14:17]
	ds_read_b128 v[110:113], v222 offset:5120
	ds_read_b128 v[194:197], v222 offset:6144
	v_mfma_f32_16x16x32_f16 v[18:21], a[108:111], v[236:239], v[18:21]
	ds_read_b128 v[202:205], v222 offset:7168
	v_mfma_f32_16x16x32_f16 v[22:25], a[140:143], v[236:239], v[22:25]
	v_mfma_f32_16x16x32_f16 v[26:29], a[172:175], v[236:239], v[26:29]
	v_mfma_f32_16x16x32_f16 v[30:33], a[204:207], v[236:239], v[30:33]
	v_mfma_f32_16x16x32_f16 v[34:37], a[236:239], v[236:239], v[34:37]
	s_cbranch_vccnz .Lrestart2
.Lfast2:
	v_mfma_f32_16x16x32_f16 v[6:9], a[16:19], v[240:243], v[6:9]
	v_and_b32_dpp v244, v70, v167 row_ror:8 row_mask:0xf bank_mask:0xf
	v_and_b32_dpp v245, v71, v167 row_ror:8 row_mask:0xf bank_mask:0xf
	v_mfma_f32_16x16x32_f16 v[10:13], a[48:51], v[240:243], v[10:13]
	v_and_b32_dpp v246, v72, v167 row_ror:8 row_mask:0xf bank_mask:0xf
	v_and_b32_dpp v247, v73, v167 row_ror:8 row_mask:0xf bank_mask:0xf
	v_mfma_f32_16x16x32_f16 v[14:17], a[80:83], v[240:243], v[14:17]
	ds_read_b128 v[162:165], v222 offset:8192
	ds_read_b128 v[158:161], v222 offset:9216
	v_mfma_f32_16x16x32_f16 v[18:21], a[112:115], v[240:243], v[18:21]
	ds_read_b128 v[154:157], v222 offset:10240
	ds_read_b128 v[150:153], v222 offset:11264
	v_mfma_f32_16x16x32_f16 v[22:25], a[144:147], v[240:243], v[22:25]
	s_waitcnt vmcnt(0)
	v_mfma_f32_16x16x32_f16 v[26:29], a[176:179], v[240:243], v[26:29]
	v_bitop3_b32 v168, v74, v75, s30 bitop3:0x7e
	v_bitop3_b32 v169, v76, v77, s30 bitop3:0x7e
	v_mfma_f32_16x16x32_f16 v[30:33], a[208:211], v[240:243], v[30:33]
	v_bitop3_b32 v168, v168, v169, s18 bitop3:0xa8
	v_cmp_ne_u32_e32 vcc, 0, v168
	v_mfma_f32_16x16x32_f16 v[34:37], a[240:243], v[240:243], v[34:37]
	v_and_b32_e32 v248, v74, v167
	v_and_b32_e32 v249, v75, v167
	v_mfma_f32_16x16x32_f16 v[6:9], a[20:23], v[244:247], v[6:9]
	v_and_b32_e32 v250, v76, v167
	v_and_b32_e32 v251, v77, v167
	v_mfma_f32_16x16x32_f16 v[10:13], a[52:55], v[244:247], v[10:13]
	ds_read_b128 v[146:149], v222 offset:12288
	ds_read_b128 v[142:145], v222 offset:13312
	v_mfma_f32_16x16x32_f16 v[14:17], a[84:87], v[244:247], v[14:17]
	ds_read_b128 v[138:141], v222 offset:14336
	ds_read_b128 v[134:137], v222 offset:15360
	v_mfma_f32_16x16x32_f16 v[18:21], a[116:119], v[244:247], v[18:21]
	v_mfma_f32_16x16x32_f16 v[22:25], a[148:151], v[244:247], v[22:25]
	v_mfma_f32_16x16x32_f16 v[26:29], a[180:183], v[244:247], v[26:29]
	v_mfma_f32_16x16x32_f16 v[30:33], a[212:215], v[244:247], v[30:33]
	v_mfma_f32_16x16x32_f16 v[34:37], a[244:247], v[244:247], v[34:37]
	s_cbranch_vccnz .Lrestart3
.Lfast3:
	v_mfma_f32_16x16x32_f16 v[6:9], a[24:27], v[248:251], v[6:9]
	v_and_b32_dpp v252, v74, v167 row_ror:8 row_mask:0xf bank_mask:0xf
	v_and_b32_dpp v253, v75, v167 row_ror:8 row_mask:0xf bank_mask:0xf
	global_load_dwordx4 v[46:49], v[4:5], off
	v_mfma_f32_16x16x32_f16 v[10:13], a[56:59], v[248:251], v[10:13]
	v_and_b32_dpp v254, v76, v167 row_ror:8 row_mask:0xf bank_mask:0xf
	v_and_b32_dpp v255, v77, v167 row_ror:8 row_mask:0xf bank_mask:0xf
	global_load_dwordx4 v[50:53], v[4:5], off offset:16
	v_mfma_f32_16x16x32_f16 v[14:17], a[88:91], v[248:251], v[14:17]
	global_load_dwordx4 v[38:41], v[4:5], off offset:128
	v_mfma_f32_16x16x32_f16 v[18:21], a[120:123], v[248:251], v[18:21]
	global_load_dwordx4 v[42:45], v[4:5], off offset:144
	v_mfma_f32_16x16x32_f16 v[22:25], a[152:155], v[248:251], v[22:25]
	s_cmp_lg_u32 s31, 0
	s_cbranch_scc1 .Lno_warm
	global_load_dwordx4 v[54:57], v[172:173], off
	global_load_dwordx4 v[58:61], v[172:173], off offset:1024

.Lrestart0:
	s_and_b64 vcc, exec, s[6:7]
	s_cbranch_vccnz .Lfast0
	buffer_load_dwordx4 v[62:65], v78, s[8:11], s28 offen sc1
	buffer_load_dwordx4 v[66:69], v78, s[8:11], s28 offen offset:1024 sc1
	buffer_load_dwordx4 v[70:73], v78, s[8:11], s28 offen offset:2048 sc1
	buffer_load_dwordx4 v[74:77], v78, s[8:11], s28 offen offset:3072 sc1
	s_add_i32 s17, s17, 1
	s_cmp_gt_u32 s17, 0x10000
	s_cselect_b64 s[6:7], -1, 0
	s_waitcnt vmcnt(3)
	v_bitop3_b32 v168, v62, v63, s30 bitop3:0x7e
	v_bitop3_b32 v169, v64, v65, s30 bitop3:0x7e
	v_bitop3_b32 v168, v168, v169, s18 bitop3:0xa8
	v_cmp_ne_u32_e32 vcc, 0, v168
	s_cbranch_vccnz .Lrestart0
	v_and_b32_e32 v224, v62, v167
	v_and_b32_e32 v225, v63, v167
	v_and_b32_e32 v226, v64, v167
	v_and_b32_e32 v227, v65, v167
	s_nop 0
	s_branch .Lfast0
.Lrestart1:
	s_and_b64 vcc, exec, s[6:7]
	s_cbranch_vccnz .Lfast1
	buffer_load_dwordx4 v[66:69], v78, s[8:11], s28 offen offset:1024 sc1
	buffer_load_dwordx4 v[70:73], v78, s[8:11], s28 offen offset:2048 sc1
	buffer_load_dwordx4 v[74:77], v78, s[8:11], s28 offen offset:3072 sc1
	s_add_i32 s17, s17, 1
	s_cmp_gt_u32 s17, 0x10000
	s_cselect_b64 s[6:7], -1, 0
	s_waitcnt vmcnt(2)
	v_bitop3_b32 v168, v66, v67, s30 bitop3:0x7e
	v_bitop3_b32 v169, v68, v69, s30 bitop3:0x7e
	v_bitop3_b32 v168, v168, v169, s18 bitop3:0xa8
	v_cmp_ne_u32_e32 vcc, 0, v168
	s_cbranch_vccnz .Lrestart1
	v_and_b32_e32 v232, v66, v167
	v_and_b32_e32 v233, v67, v167
	v_and_b32_e32 v234, v68, v167
	v_and_b32_e32 v235, v69, v167
	s_nop 0
	s_branch .Lfast1
.Lrestart2:
	s_and_b64 vcc, exec, s[6:7]
	s_cbranch_vccnz .Lfast2
	buffer_load_dwordx4 v[70:73], v78, s[8:11], s28 offen offset:2048 sc1
	buffer_load_dwordx4 v[74:77], v78, s[8:11], s28 offen offset:3072 sc1
	s_add_i32 s17, s17, 1
	s_cmp_gt_u32 s17, 0x10000
	s_cselect_b64 s[6:7], -1, 0
	s_waitcnt vmcnt(1)
	v_bitop3_b32 v168, v70, v71, s30 bitop3:0x7e
	v_bitop3_b32 v169, v72, v73, s30 bitop3:0x7e
	v_bitop3_b32 v168, v168, v169, s18 bitop3:0xa8
	v_cmp_ne_u32_e32 vcc, 0, v168
	s_cbranch_vccnz .Lrestart2
	v_and_b32_e32 v240, v70, v167
	v_and_b32_e32 v241, v71, v167
	v_and_b32_e32 v242, v72, v167
	v_and_b32_e32 v243, v73, v167
	s_nop 0
	s_branch .Lfast2
.Lrestart3:
	s_and_b64 vcc, exec, s[6:7]
	s_cbranch_vccnz .Lfast3
	buffer_load_dwordx4 v[74:77], v78, s[8:11], s28 offen offset:3072 sc1
	s_add_i32 s17, s17, 1
	s_cmp_gt_u32 s17, 0x10000
	s_cselect_b64 s[6:7], -1, 0
	s_waitcnt vmcnt(0)
	v_bitop3_b32 v168, v74, v75, s30 bitop3:0x7e
	v_bitop3_b32 v169, v76, v77, s30 bitop3:0x7e
	v_bitop3_b32 v168, v168, v169, s18 bitop3:0xa8
	v_cmp_ne_u32_e32 vcc, 0, v168
	s_cbranch_vccnz .Lrestart3
	v_and_b32_e32 v248, v74, v167
	v_and_b32_e32 v249, v75, v167
	v_and_b32_e32 v250, v76, v167
	v_and_b32_e32 v251, v77, v167
	s_nop 0
	s_branch .Lfast3
